# grid-barrier spin loops poll without the s_sleep between polls
# speedup vs baseline: 1.0016x; 1.0016x over previous
; __device__ __forceinline__ unsigned xb_ld(unsigned* p)              { return __hip_atomic_load(p, __ATOMIC_RELAXED, __HIP_MEMORY_SCOPE_AGENT); }
; __device__ __forceinline__ void xcd_barrier_complete(unsigned* bar, unsigned x, unsigned& nloc, unsigned& nx) {
;     const unsigned G = gridDim.x * gridDim.y * gridDim.z;
;     unsigned sum, cnt, mine, sp = 0u;
;     for (;;) {
;         sum = 0u; cnt = 0u; mine = 0u;
; #pragma unroll
;         for (unsigned j = 0; j < 16; ++j) { const unsigned c = xb_ld(&bar[XB_XCNT(j)]); sum += c; cnt += (c > 0u) ? 1u : 0u; mine = (j == x) ? c : mine; }
;         if (sum == G) break;
;         __builtin_amdgcn_s_sleep(1);
;         if ((++sp & 255u) == 0u) { if (xb_ld(&bar[XB_TMO])) break; if (sp > XB_SPIN_CAP) { atomicAdd(&bar[XB_TMO], 1u); break; } }
;     }
;     nloc = mine > 0u ? mine : 1u; nx = cnt > 0u ? cnt : 1u;
; }
.LBB0_103:
	global_load_dword v15, v16, s[8:9] sc1
	global_load_dword v0, v16, s[12:13] sc1
	global_load_dword v1, v16, s[14:15] sc1
	global_load_dword v2, v16, s[16:17] sc1
	global_load_dword v3, v16, s[18:19] sc1
	global_load_dword v4, v16, s[20:21] sc1
	global_load_dword v5, v16, s[22:23] sc1
	global_load_dword v6, v16, s[24:25] sc1
	global_load_dword v7, v16, s[26:27] sc1
	global_load_dword v8, v16, s[28:29] sc1
	global_load_dword v9, v16, s[30:31] sc1
	global_load_dword v10, v16, s[34:35] sc1
	global_load_dword v11, v16, s[36:37] sc1
	global_load_dword v12, v16, s[38:39] sc1
	global_load_dword v13, v16, s[40:41] sc1
	global_load_dword v14, v16, s[42:43] sc1
	s_mov_b64 s[44:45], -1
	s_mov_b64 s[46:47], -1
	s_waitcnt vmcnt(14)
	v_add_u32_e32 v17, v0, v15
	s_waitcnt vmcnt(13)
	v_add_u32_e32 v17, v17, v1
	s_waitcnt vmcnt(12)
	v_add_u32_e32 v17, v17, v2
	s_waitcnt vmcnt(11)
	v_add_u32_e32 v17, v17, v3
	s_waitcnt vmcnt(10)
	v_add_u32_e32 v17, v17, v4
	s_waitcnt vmcnt(9)
	v_add_u32_e32 v17, v17, v5
	s_waitcnt vmcnt(8)
	v_add_u32_e32 v17, v17, v6
	s_waitcnt vmcnt(7)
	v_add_u32_e32 v17, v17, v7
	s_waitcnt vmcnt(6)
	v_add_u32_e32 v17, v17, v8
	s_waitcnt vmcnt(5)
	v_add_u32_e32 v17, v17, v9
	s_waitcnt vmcnt(4)
	v_add_u32_e32 v17, v17, v10
	s_waitcnt vmcnt(3)
	v_add_u32_e32 v17, v17, v11
	s_waitcnt vmcnt(2)
	v_add_u32_e32 v17, v17, v12
	s_waitcnt vmcnt(1)
	v_add_u32_e32 v17, v17, v13
	s_waitcnt vmcnt(0)
	v_add_u32_e32 v17, v17, v14
	v_cmp_eq_u32_e32 vcc, s1, v17
	s_cbranch_vccnz .LBB0_102
	s_and_b32 s3, s2, 0xff
	s_cmp_eq_u32 s3, 0
	s_mov_b64 s[48:49], -1
	s_nop 0
	s_cbranch_scc1 .LBB0_107
	s_and_b64 vcc, exec, s[48:49]
	s_cbranch_vccz .LBB0_102

.LBB0_121:
	s_and_b32 s2, s1, 0xff
	s_mov_b64 s[22:23], -1
	s_cmp_lg_u32 s2, 0
	s_mov_b64 s[26:27], -1
	s_nop 0
	s_cbranch_scc0 .LBB0_124
	s_and_b64 vcc, exec, s[26:27]
	s_cbranch_vccz .LBB0_120

.LBB0_138:
	s_and_b32 s2, s1, 0xff
	s_cmp_lg_u32 s2, 0
	s_mov_b64 s[24:25], -1
	s_nop 0
	s_cbranch_scc0 .LBB0_141
	s_mov_b64 s[26:27], -1
	s_and_b64 vcc, exec, s[24:25]
	s_cbranch_vccz .LBB0_137

; __device__ __forceinline__ unsigned xb_ld(unsigned* p)              { return __hip_atomic_load(p, __ATOMIC_RELAXED, __HIP_MEMORY_SCOPE_AGENT); }
; __device__ __forceinline__ void xcd_barrier_complete(unsigned* bar, unsigned x, unsigned& nloc, unsigned& nx) {
;     const unsigned G = gridDim.x * gridDim.y * gridDim.z;
;     unsigned sum, cnt, mine, sp = 0u;
;     for (;;) {
;         sum = 0u; cnt = 0u; mine = 0u;
; #pragma unroll
;         for (unsigned j = 0; j < 16; ++j) { const unsigned c = xb_ld(&bar[XB_XCNT(j)]); sum += c; cnt += (c > 0u) ? 1u : 0u; mine = (j == x) ? c : mine; }
;         if (sum == G) break;
;         __builtin_amdgcn_s_sleep(1);
;         if ((++sp & 255u) == 0u) { if (xb_ld(&bar[XB_TMO])) break; if (sp > XB_SPIN_CAP) { atomicAdd(&bar[XB_TMO], 1u); break; } }
;     }
;     nloc = mine > 0u ? mine : 1u; nx = cnt > 0u ? cnt : 1u;
; }
.LBB0_237:
	v_readlane_b32 s6, v252, 7
	v_readlane_b32 s7, v252, 8
	global_load_dword v0, v80, s[84:85] sc1
	s_mov_b64 s[8:9], -1
	s_nop 2
	global_load_dword v1, v80, s[6:7] sc1
	v_readlane_b32 s6, v252, 9
	v_readlane_b32 s7, v252, 10
	s_waitcnt vmcnt(0)
	v_add_u32_e32 v16, v1, v0
	s_nop 2
	global_load_dword v2, v80, s[6:7] sc1
	v_readlane_b32 s6, v252, 11
	v_readlane_b32 s7, v252, 12
	s_waitcnt vmcnt(0)
	v_add_u32_e32 v16, v16, v2
	s_nop 2
	global_load_dword v3, v80, s[6:7] sc1
	v_readlane_b32 s6, v252, 13
	v_readlane_b32 s7, v252, 14
	s_waitcnt vmcnt(0)
	v_add_u32_e32 v16, v16, v3
	s_nop 2
	global_load_dword v4, v80, s[6:7] sc1
	v_readlane_b32 s6, v252, 15
	v_readlane_b32 s7, v252, 16
	s_waitcnt vmcnt(0)
	v_add_u32_e32 v16, v16, v4
	s_nop 2
	global_load_dword v5, v80, s[6:7] sc1
	v_readlane_b32 s6, v252, 17
	v_readlane_b32 s7, v252, 18
	s_waitcnt vmcnt(0)
	v_add_u32_e32 v16, v16, v5
	s_nop 2
	global_load_dword v6, v80, s[6:7] sc1
	v_readlane_b32 s6, v252, 19
	v_readlane_b32 s7, v252, 20
	s_waitcnt vmcnt(0)
	v_add_u32_e32 v16, v16, v6
	s_nop 2
	global_load_dword v7, v80, s[6:7] sc1
	v_readlane_b32 s6, v252, 21
	v_readlane_b32 s7, v252, 22
	s_waitcnt vmcnt(0)
	v_add_u32_e32 v16, v16, v7
	s_nop 2
	global_load_dword v8, v80, s[6:7] sc1
	v_readlane_b32 s6, v252, 23
	v_readlane_b32 s7, v252, 24
	s_waitcnt vmcnt(0)
	v_add_u32_e32 v16, v16, v8
	s_nop 2
	global_load_dword v9, v80, s[6:7] sc1
	v_readlane_b32 s6, v252, 25
	v_readlane_b32 s7, v252, 26
	s_waitcnt vmcnt(0)
	v_add_u32_e32 v16, v16, v9
	s_nop 2
	global_load_dword v10, v80, s[6:7] sc1
	v_readlane_b32 s6, v252, 27
	v_readlane_b32 s7, v252, 28
	s_waitcnt vmcnt(0)
	v_add_u32_e32 v16, v16, v10
	s_nop 2
	global_load_dword v11, v80, s[6:7] sc1
	v_readlane_b32 s6, v252, 29
	v_readlane_b32 s7, v252, 30
	s_waitcnt vmcnt(0)
	v_add_u32_e32 v16, v16, v11
	s_nop 2
	global_load_dword v12, v80, s[6:7] sc1
	v_readlane_b32 s6, v252, 31
	v_readlane_b32 s7, v252, 32
	s_waitcnt vmcnt(0)
	v_add_u32_e32 v16, v16, v12
	s_nop 2
	global_load_dword v13, v80, s[6:7] sc1
	v_readlane_b32 s6, v252, 33
	v_readlane_b32 s7, v252, 34
	s_waitcnt vmcnt(0)
	v_add_u32_e32 v16, v16, v13
	s_nop 2
	global_load_dword v14, v80, s[6:7] sc1
	v_readlane_b32 s6, v252, 35
	v_readlane_b32 s7, v252, 36
	s_waitcnt vmcnt(0)
	v_add_u32_e32 v16, v16, v14
	s_nop 2
	global_load_dword v15, v80, s[6:7] sc1
	s_mov_b64 s[6:7], -1
	s_waitcnt vmcnt(0)
	v_add_u32_e32 v16, v16, v15
	v_cmp_eq_u32_e32 vcc, s12, v16
	s_cbranch_vccnz .LBB0_236
	s_and_b32 s6, s13, 0xff
	s_cmp_eq_u32 s6, 0
	s_mov_b64 s[6:7], -1
	s_mov_b64 s[10:11], -1
	s_nop 0
	s_cbranch_scc1 .LBB0_241
	s_and_b64 vcc, exec, s[10:11]
	s_cbranch_vccz .LBB0_236

.LBB0_255:
	s_and_b32 s16, s23, 0xff
	s_mov_b64 s[14:15], -1
	s_cmp_lg_u32 s16, 0
	s_mov_b64 s[18:19], -1
	s_nop 0
	s_cbranch_scc0 .LBB0_258
	s_and_b64 vcc, exec, s[18:19]
	s_cbranch_vccz .LBB0_254

.LBB0_1637:
	s_and_b32 s16, s22, 0xff
	s_mov_b64 s[14:15], -1
	s_cmp_lg_u32 s16, 0
	s_mov_b64 s[18:19], -1
	s_nop 0
	s_cbranch_scc0 .LBB0_1640
	s_and_b64 vcc, exec, s[18:19]
	s_cbranch_vccz .LBB0_1636
